# modulate0 loop hand-rewritten: two rows per iteration sharing the modulation vectors; 40 bytes of unreachable padding
# baseline (speedup 1.0000x reference)
.LBB0_291:
	s_cmp_lt_i32 s86, 2
	s_cselect_b64 s[0:1], -1, 0
	s_and_b64 s[0:1], s[0:1], s[4:5]
	s_andn2_b64 vcc, exec, s[0:1]
	s_cbranch_vccnz .LBB0_310
	v_readlane_b32 s2, v255, 25
	s_cmpk_gt_i32 s2, 0x43ff
	v_readlane_b32 s3, v255, 26
	s_cbranch_scc1 .LBB0_297
	s_add_u32 s2, s84, 0x100000
	s_addc_u32 s18, s85, 0
	s_add_u32 s19, s84, 0x25300000
	v_readlane_b32 s4, v255, 25
	s_addc_u32 s20, s85, 0
	v_readlane_b32 s5, v255, 26
	s_mov_b32 s12, s4
	s_ashr_i32 s13, s4, 31
	s_ashr_i32 s93, s92, 31
	s_lshl_b64 s[4:5], s[12:13], 13
	s_mov_b32 s9, 0
	s_mov_b32 s8, s12
	s_add_u32 s4, s68, s4
	v_writelane_b32 v255, s8, 25
	v_lshlrev_b32_e32 v2, 2, v1
	s_addc_u32 s5, s69, s5
	s_lshl_b64 s[6:7], s[92:93], 13
	s_mov_b64 s[10:11], 0x2000
	s_movk_i32 s21, 0x1000
	s_movk_i32 s22, 0x3000
	v_writelane_b32 v255, s9, 26
	s_cmpk_lg_i32 s92, 0x800
	s_cbranch_scc1 .LBB0_295
	v_lshlrev_b32_e32 v4, 2, v2
	v_lshlrev_b32_e32 v5, 1, v2
	s_mov_b32 s14, s2
	s_mov_b32 s15, s18
	s_add_u32 s8, s4, 0x1000000
	s_addc_u32 s9, s5, 0
	s_lshl_b64 s[16:17], s[12:13], 12
	s_add_u32 s16, s16, s19
	s_addc_u32 s17, s17, s20
	s_add_u32 s10, s16, 0x800000
	s_addc_u32 s11, s17, 0
	s_mov_b32 s21, 4
.Lmod2_loop:
	s_add_u32 s24, s4, 0x1000
	s_addc_u32 s25, s5, 0
	global_load_dwordx4 v[6:9], v4, s[4:5] nt
	global_load_dwordx4 v[10:13], v4, s[4:5] offset:1024 nt
	global_load_dwordx4 v[14:17], v4, s[4:5] offset:2048 nt
	global_load_dwordx4 v[18:21], v4, s[4:5] offset:3072 nt
	global_load_dwordx4 v[22:25], v4, s[24:25] nt
	global_load_dwordx4 v[26:29], v4, s[24:25] offset:1024 nt
	global_load_dwordx4 v[30:33], v4, s[24:25] offset:2048 nt
	global_load_dwordx4 v[34:37], v4, s[24:25] offset:3072 nt
	s_add_u32 s24, s8, 0x1000
	s_addc_u32 s25, s9, 0
	global_load_dwordx4 v[38:41], v4, s[8:9] nt
	global_load_dwordx4 v[42:45], v4, s[8:9] offset:1024 nt
	global_load_dwordx4 v[46:49], v4, s[8:9] offset:2048 nt
	global_load_dwordx4 v[50:53], v4, s[8:9] offset:3072 nt
	global_load_dwordx4 v[54:57], v4, s[24:25] nt
	global_load_dwordx4 v[58:61], v4, s[24:25] offset:1024 nt
	global_load_dwordx4 v[62:65], v4, s[24:25] offset:2048 nt
	global_load_dwordx4 v[66:69], v4, s[24:25] offset:3072 nt
	s_add_u32 s2, s14, 0x0
	s_addc_u32 s3, s15, 0
	s_add_u32 s22, s14, 0x2000
	s_addc_u32 s23, s15, 0
	global_load_dwordx4 v[70:73], v4, s[2:3]
	global_load_dwordx4 v[86:89], v4, s[22:23]
	global_load_dwordx4 v[74:77], v4, s[2:3] offset:1024
	global_load_dwordx4 v[90:93], v4, s[22:23] offset:1024
	global_load_dwordx4 v[78:81], v4, s[2:3] offset:2048
	global_load_dwordx4 v[94:97], v4, s[22:23] offset:2048
	global_load_dwordx4 v[82:85], v4, s[2:3] offset:3072
	global_load_dwordx4 v[98:101], v4, s[22:23] offset:3072
	s_waitcnt vmcnt(6)
	v_pk_add_f32 v[86:87], v[86:87], 1.0 op_sel_hi:[1,0]
	v_pk_add_f32 v[88:89], v[88:89], 1.0 op_sel_hi:[1,0]
	v_pk_fma_f32 v[6:7], v[6:7], v[86:87], v[70:71]
	v_pk_fma_f32 v[8:9], v[8:9], v[88:89], v[72:73]
	v_pk_fma_f32 v[38:39], v[38:39], v[86:87], v[70:71]
	v_pk_fma_f32 v[40:41], v[40:41], v[88:89], v[72:73]
	v_cvt_pk_bf16_f32 v6, v6, v7
	v_cvt_pk_bf16_f32 v7, v8, v9
	v_cvt_pk_bf16_f32 v38, v38, v39
	v_cvt_pk_bf16_f32 v39, v40, v41
	s_waitcnt vmcnt(4)
	v_pk_add_f32 v[90:91], v[90:91], 1.0 op_sel_hi:[1,0]
	v_pk_add_f32 v[92:93], v[92:93], 1.0 op_sel_hi:[1,0]
	v_pk_fma_f32 v[10:11], v[10:11], v[90:91], v[74:75]
	v_pk_fma_f32 v[12:13], v[12:13], v[92:93], v[76:77]
	v_pk_fma_f32 v[42:43], v[42:43], v[90:91], v[74:75]
	v_pk_fma_f32 v[44:45], v[44:45], v[92:93], v[76:77]
	v_cvt_pk_bf16_f32 v10, v10, v11
	v_cvt_pk_bf16_f32 v11, v12, v13
	v_cvt_pk_bf16_f32 v42, v42, v43
	v_cvt_pk_bf16_f32 v43, v44, v45
	s_waitcnt vmcnt(2)
	v_pk_add_f32 v[94:95], v[94:95], 1.0 op_sel_hi:[1,0]
	v_pk_add_f32 v[96:97], v[96:97], 1.0 op_sel_hi:[1,0]
	v_pk_fma_f32 v[14:15], v[14:15], v[94:95], v[78:79]
	v_pk_fma_f32 v[16:17], v[16:17], v[96:97], v[80:81]
	v_pk_fma_f32 v[46:47], v[46:47], v[94:95], v[78:79]
	v_pk_fma_f32 v[48:49], v[48:49], v[96:97], v[80:81]
	v_cvt_pk_bf16_f32 v14, v14, v15
	v_cvt_pk_bf16_f32 v15, v16, v17
	v_cvt_pk_bf16_f32 v46, v46, v47
	v_cvt_pk_bf16_f32 v47, v48, v49
	s_waitcnt vmcnt(0)
	v_pk_add_f32 v[98:99], v[98:99], 1.0 op_sel_hi:[1,0]
	v_pk_add_f32 v[100:101], v[100:101], 1.0 op_sel_hi:[1,0]
	v_pk_fma_f32 v[18:19], v[18:19], v[98:99], v[82:83]
	v_pk_fma_f32 v[20:21], v[20:21], v[100:101], v[84:85]
	v_pk_fma_f32 v[50:51], v[50:51], v[98:99], v[82:83]
	v_pk_fma_f32 v[52:53], v[52:53], v[100:101], v[84:85]
	v_cvt_pk_bf16_f32 v18, v18, v19
	v_cvt_pk_bf16_f32 v19, v20, v21
	v_cvt_pk_bf16_f32 v50, v50, v51
	v_cvt_pk_bf16_f32 v51, v52, v53
	s_add_u32 s2, s14, 0x1000
	s_addc_u32 s3, s15, 0
	s_add_u32 s22, s14, 0x3000
	s_addc_u32 s23, s15, 0
	global_load_dwordx4 v[70:73], v4, s[2:3]
	global_load_dwordx4 v[86:89], v4, s[22:23]
	global_load_dwordx4 v[74:77], v4, s[2:3] offset:1024
	global_load_dwordx4 v[90:93], v4, s[22:23] offset:1024
	global_load_dwordx4 v[78:81], v4, s[2:3] offset:2048
	global_load_dwordx4 v[94:97], v4, s[22:23] offset:2048
	global_load_dwordx4 v[82:85], v4, s[2:3] offset:3072
	global_load_dwordx4 v[98:101], v4, s[22:23] offset:3072
	s_waitcnt vmcnt(6)
	v_pk_add_f32 v[86:87], v[86:87], 1.0 op_sel_hi:[1,0]
	v_pk_add_f32 v[88:89], v[88:89], 1.0 op_sel_hi:[1,0]
	v_pk_fma_f32 v[22:23], v[22:23], v[86:87], v[70:71]
	v_pk_fma_f32 v[24:25], v[24:25], v[88:89], v[72:73]
	v_pk_fma_f32 v[54:55], v[54:55], v[86:87], v[70:71]
	v_pk_fma_f32 v[56:57], v[56:57], v[88:89], v[72:73]
	v_cvt_pk_bf16_f32 v22, v22, v23
	v_cvt_pk_bf16_f32 v23, v24, v25
	v_cvt_pk_bf16_f32 v54, v54, v55
	v_cvt_pk_bf16_f32 v55, v56, v57
	s_waitcnt vmcnt(4)
	v_pk_add_f32 v[90:91], v[90:91], 1.0 op_sel_hi:[1,0]
	v_pk_add_f32 v[92:93], v[92:93], 1.0 op_sel_hi:[1,0]
	v_pk_fma_f32 v[26:27], v[26:27], v[90:91], v[74:75]
	v_pk_fma_f32 v[28:29], v[28:29], v[92:93], v[76:77]
	v_pk_fma_f32 v[58:59], v[58:59], v[90:91], v[74:75]
	v_pk_fma_f32 v[60:61], v[60:61], v[92:93], v[76:77]
	v_cvt_pk_bf16_f32 v26, v26, v27
	v_cvt_pk_bf16_f32 v27, v28, v29
	v_cvt_pk_bf16_f32 v58, v58, v59
	v_cvt_pk_bf16_f32 v59, v60, v61
	s_waitcnt vmcnt(2)
	v_pk_add_f32 v[94:95], v[94:95], 1.0 op_sel_hi:[1,0]
	v_pk_add_f32 v[96:97], v[96:97], 1.0 op_sel_hi:[1,0]
	v_pk_fma_f32 v[30:31], v[30:31], v[94:95], v[78:79]
	v_pk_fma_f32 v[32:33], v[32:33], v[96:97], v[80:81]
	v_pk_fma_f32 v[62:63], v[62:63], v[94:95], v[78:79]
	v_pk_fma_f32 v[64:65], v[64:65], v[96:97], v[80:81]
	v_cvt_pk_bf16_f32 v30, v30, v31
	v_cvt_pk_bf16_f32 v31, v32, v33
	v_cvt_pk_bf16_f32 v62, v62, v63
	v_cvt_pk_bf16_f32 v63, v64, v65
	s_waitcnt vmcnt(0)
	v_pk_add_f32 v[98:99], v[98:99], 1.0 op_sel_hi:[1,0]
	v_pk_add_f32 v[100:101], v[100:101], 1.0 op_sel_hi:[1,0]
	v_pk_fma_f32 v[34:35], v[34:35], v[98:99], v[82:83]
	v_pk_fma_f32 v[36:37], v[36:37], v[100:101], v[84:85]
	v_pk_fma_f32 v[66:67], v[66:67], v[98:99], v[82:83]
	v_pk_fma_f32 v[68:69], v[68:69], v[100:101], v[84:85]
	v_cvt_pk_bf16_f32 v34, v34, v35
	v_cvt_pk_bf16_f32 v35, v36, v37
	v_cvt_pk_bf16_f32 v66, v66, v67
	v_cvt_pk_bf16_f32 v67, v68, v69
	global_store_dwordx2 v5, v[6:7], s[16:17]
	global_store_dwordx2 v5, v[38:39], s[10:11]
	global_store_dwordx2 v5, v[10:11], s[16:17] offset:512
	global_store_dwordx2 v5, v[42:43], s[10:11] offset:512
	global_store_dwordx2 v5, v[14:15], s[16:17] offset:1024
	global_store_dwordx2 v5, v[46:47], s[10:11] offset:1024
	global_store_dwordx2 v5, v[18:19], s[16:17] offset:1536
	global_store_dwordx2 v5, v[50:51], s[10:11] offset:1536
	global_store_dwordx2 v5, v[22:23], s[16:17] offset:2048
	global_store_dwordx2 v5, v[54:55], s[10:11] offset:2048
	global_store_dwordx2 v5, v[26:27], s[16:17] offset:2560
	global_store_dwordx2 v5, v[58:59], s[10:11] offset:2560
	global_store_dwordx2 v5, v[30:31], s[16:17] offset:3072
	global_store_dwordx2 v5, v[62:63], s[10:11] offset:3072
	global_store_dwordx2 v5, v[34:35], s[16:17] offset:3584
	global_store_dwordx2 v5, v[66:67], s[10:11] offset:3584
	s_add_u32 s4, s4, 0x2000000
	s_addc_u32 s5, s5, 0
	s_add_u32 s8, s8, 0x2000000
	s_addc_u32 s9, s9, 0
	s_add_u32 s16, s16, 0x1000000
	s_addc_u32 s17, s17, 0
	s_add_u32 s10, s10, 0x1000000
	s_addc_u32 s11, s11, 0
	s_add_u32 s14, s14, 0xc000
	s_addc_u32 s15, s15, 0
	s_add_i32 s21, s21, -1
	s_cmp_lg_u32 s21, 0
	s_cbranch_scc1 .Lmod2_loop
	s_cmpk_gt_i32 s12, 0x3ff
	s_cbranch_scc1 .LBB0_297
	s_lshl_b64 s[4:5], s[12:13], 13
	s_add_u32 s4, s72, s4
	s_addc_u32 s5, s73, s5
	s_add_u32 s24, s4, 0x1000
	s_addc_u32 s25, s5, 0
	global_load_dwordx4 v[6:9], v4, s[4:5] nt
	global_load_dwordx4 v[10:13], v4, s[4:5] offset:1024 nt
	global_load_dwordx4 v[14:17], v4, s[4:5] offset:2048 nt
	global_load_dwordx4 v[18:21], v4, s[4:5] offset:3072 nt
	global_load_dwordx4 v[22:25], v4, s[24:25] nt
	global_load_dwordx4 v[26:29], v4, s[24:25] offset:1024 nt
	global_load_dwordx4 v[30:33], v4, s[24:25] offset:2048 nt
	global_load_dwordx4 v[34:37], v4, s[24:25] offset:3072 nt
	s_add_u32 s2, s14, 0x0
	s_addc_u32 s3, s15, 0
	s_add_u32 s22, s14, 0x2000
	s_addc_u32 s23, s15, 0
	global_load_dwordx4 v[70:73], v4, s[2:3]
	global_load_dwordx4 v[86:89], v4, s[22:23]
	global_load_dwordx4 v[74:77], v4, s[2:3] offset:1024
	global_load_dwordx4 v[90:93], v4, s[22:23] offset:1024
	global_load_dwordx4 v[78:81], v4, s[2:3] offset:2048
	global_load_dwordx4 v[94:97], v4, s[22:23] offset:2048
	global_load_dwordx4 v[82:85], v4, s[2:3] offset:3072
	global_load_dwordx4 v[98:101], v4, s[22:23] offset:3072
	s_waitcnt vmcnt(6)
	v_pk_add_f32 v[86:87], v[86:87], 1.0 op_sel_hi:[1,0]
	v_pk_add_f32 v[88:89], v[88:89], 1.0 op_sel_hi:[1,0]
	v_pk_fma_f32 v[6:7], v[6:7], v[86:87], v[70:71]
	v_pk_fma_f32 v[8:9], v[8:9], v[88:89], v[72:73]
	v_cvt_pk_bf16_f32 v6, v6, v7
	v_cvt_pk_bf16_f32 v7, v8, v9
	s_waitcnt vmcnt(4)
	v_pk_add_f32 v[90:91], v[90:91], 1.0 op_sel_hi:[1,0]
	v_pk_add_f32 v[92:93], v[92:93], 1.0 op_sel_hi:[1,0]
	v_pk_fma_f32 v[10:11], v[10:11], v[90:91], v[74:75]
	v_pk_fma_f32 v[12:13], v[12:13], v[92:93], v[76:77]
	v_cvt_pk_bf16_f32 v10, v10, v11
	v_cvt_pk_bf16_f32 v11, v12, v13
	s_waitcnt vmcnt(2)
	v_pk_add_f32 v[94:95], v[94:95], 1.0 op_sel_hi:[1,0]
	v_pk_add_f32 v[96:97], v[96:97], 1.0 op_sel_hi:[1,0]
	v_pk_fma_f32 v[14:15], v[14:15], v[94:95], v[78:79]
	v_pk_fma_f32 v[16:17], v[16:17], v[96:97], v[80:81]
	v_cvt_pk_bf16_f32 v14, v14, v15
	v_cvt_pk_bf16_f32 v15, v16, v17
	s_waitcnt vmcnt(0)
	v_pk_add_f32 v[98:99], v[98:99], 1.0 op_sel_hi:[1,0]
	v_pk_add_f32 v[100:101], v[100:101], 1.0 op_sel_hi:[1,0]
	v_pk_fma_f32 v[18:19], v[18:19], v[98:99], v[82:83]
	v_pk_fma_f32 v[20:21], v[20:21], v[100:101], v[84:85]
	v_cvt_pk_bf16_f32 v18, v18, v19
	v_cvt_pk_bf16_f32 v19, v20, v21
	s_add_u32 s2, s14, 0x1000
	s_addc_u32 s3, s15, 0
	s_add_u32 s22, s14, 0x3000
	s_addc_u32 s23, s15, 0
	global_load_dwordx4 v[70:73], v4, s[2:3]
	global_load_dwordx4 v[86:89], v4, s[22:23]
	global_load_dwordx4 v[74:77], v4, s[2:3] offset:1024
	global_load_dwordx4 v[90:93], v4, s[22:23] offset:1024
	global_load_dwordx4 v[78:81], v4, s[2:3] offset:2048
	global_load_dwordx4 v[94:97], v4, s[22:23] offset:2048
	global_load_dwordx4 v[82:85], v4, s[2:3] offset:3072
	global_load_dwordx4 v[98:101], v4, s[22:23] offset:3072
	s_waitcnt vmcnt(6)
	v_pk_add_f32 v[86:87], v[86:87], 1.0 op_sel_hi:[1,0]
	v_pk_add_f32 v[88:89], v[88:89], 1.0 op_sel_hi:[1,0]
	v_pk_fma_f32 v[22:23], v[22:23], v[86:87], v[70:71]
	v_pk_fma_f32 v[24:25], v[24:25], v[88:89], v[72:73]
	v_cvt_pk_bf16_f32 v22, v22, v23
	v_cvt_pk_bf16_f32 v23, v24, v25
	s_waitcnt vmcnt(4)
	v_pk_add_f32 v[90:91], v[90:91], 1.0 op_sel_hi:[1,0]
	v_pk_add_f32 v[92:93], v[92:93], 1.0 op_sel_hi:[1,0]
	v_pk_fma_f32 v[26:27], v[26:27], v[90:91], v[74:75]
	v_pk_fma_f32 v[28:29], v[28:29], v[92:93], v[76:77]
	v_cvt_pk_bf16_f32 v26, v26, v27
	v_cvt_pk_bf16_f32 v27, v28, v29
	s_waitcnt vmcnt(2)
	v_pk_add_f32 v[94:95], v[94:95], 1.0 op_sel_hi:[1,0]
	v_pk_add_f32 v[96:97], v[96:97], 1.0 op_sel_hi:[1,0]
	v_pk_fma_f32 v[30:31], v[30:31], v[94:95], v[78:79]
	v_pk_fma_f32 v[32:33], v[32:33], v[96:97], v[80:81]
	v_cvt_pk_bf16_f32 v30, v30, v31
	v_cvt_pk_bf16_f32 v31, v32, v33
	s_waitcnt vmcnt(0)
	v_pk_add_f32 v[98:99], v[98:99], 1.0 op_sel_hi:[1,0]
	v_pk_add_f32 v[100:101], v[100:101], 1.0 op_sel_hi:[1,0]
	v_pk_fma_f32 v[34:35], v[34:35], v[98:99], v[82:83]
	v_pk_fma_f32 v[36:37], v[36:37], v[100:101], v[84:85]
	v_cvt_pk_bf16_f32 v34, v34, v35
	v_cvt_pk_bf16_f32 v35, v36, v37
	global_store_dwordx2 v5, v[6:7], s[16:17]
	global_store_dwordx2 v5, v[10:11], s[16:17] offset:512
	global_store_dwordx2 v5, v[14:15], s[16:17] offset:1024
	global_store_dwordx2 v5, v[18:19], s[16:17] offset:1536
	global_store_dwordx2 v5, v[22:23], s[16:17] offset:2048
	global_store_dwordx2 v5, v[26:27], s[16:17] offset:2560
	global_store_dwordx2 v5, v[30:31], s[16:17] offset:3072
	global_store_dwordx2 v5, v[34:35], s[16:17] offset:3584
	s_branch .LBB0_297
	s_nop 0
	s_nop 0
	s_nop 0
	s_nop 0
	s_nop 0
	s_nop 0
	s_nop 0
	s_nop 0
	s_nop 0
	s_nop 0
